# step dispatches (scalar compare) to a variant without the second K-half select ops and MFMAs when the block ends in the first half; heads kept at 4 mod 8
# speedup vs baseline: 1.0008x; 1.0004x over previous
.Lcs_done:
	global_load_dword v241, v4, s[54:55]
	s_add_i32 s18, s13, 32
	s_add_i32 s19, s13, 16
	s_mov_b64 s[6:7], 0
	s_cmp_ge_i32 s19, s71
	s_cbranch_scc1 .Lstep_h0
	v_mfma_f32_32x32x16_f16 v[82:97], v[194:197], v[178:181], 0
	v_mfma_f32_32x32x16_f16 v[98:113], v[194:197], v[182:185], 0
	v_add_u32_e32 v14, s13, v243
	v_sub_u32_e32 v3, v230, v14
	v_add_u32_e32 v4, v3, v234
	v_add_u32_e32 v5, -1, v3
	v_med3_i32 v4, v4, -1, 32
	v_med3_i32 v5, v5, -1, 32
	v_cvt_f32_i32_e32 v4, v4
	v_cvt_f32_i32_e32 v5, v5
	v_cvt_pk_f16_f32 v14, v4, v4
	v_cvt_pk_f16_f32 v15, v5, v5
	v_pk_add_f16 v3, v14, s73 neg_lo:[0,1] neg_hi:[0,1]
	v_pk_add_f16 v4, s73, v15 neg_lo:[0,1] neg_hi:[0,1]
	v_pk_min_f16 v6, v3, v4 clamp
	v_pk_add_f16 v5, v14, s74 neg_lo:[0,1] neg_hi:[0,1]
	v_pk_add_f16 v16, s74, v15 neg_lo:[0,1] neg_hi:[0,1]
	v_pk_min_f16 v7, v5, v16 clamp
	v_pk_add_f16 v3, v14, s75 neg_lo:[0,1] neg_hi:[0,1]
	v_pk_add_f16 v4, s75, v15 neg_lo:[0,1] neg_hi:[0,1]
	v_pk_min_f16 v8, v3, v4 clamp
	v_pk_add_f16 v5, v14, s76 neg_lo:[0,1] neg_hi:[0,1]
	v_pk_add_f16 v16, s76, v15 neg_lo:[0,1] neg_hi:[0,1]
	v_pk_min_f16 v9, v5, v16 clamp
	v_pk_add_f16 v3, v14, s77 neg_lo:[0,1] neg_hi:[0,1]
	v_pk_add_f16 v4, s77, v15 neg_lo:[0,1] neg_hi:[0,1]
	v_pk_min_f16 v10, v3, v4 clamp
	v_pk_add_f16 v5, v14, s78 neg_lo:[0,1] neg_hi:[0,1]
	v_pk_add_f16 v16, s78, v15 neg_lo:[0,1] neg_hi:[0,1]
	v_pk_min_f16 v11, v5, v16 clamp
	v_pk_add_f16 v3, v14, s79 neg_lo:[0,1] neg_hi:[0,1]
	v_pk_add_f16 v4, s79, v15 neg_lo:[0,1] neg_hi:[0,1]
	v_pk_min_f16 v12, v3, v4 clamp
	v_pk_add_f16 v5, v14, s80 neg_lo:[0,1] neg_hi:[0,1]
	v_pk_add_f16 v16, s80, v15 neg_lo:[0,1] neg_hi:[0,1]
	v_pk_min_f16 v13, v5, v16 clamp
	v_exp_f32_e32 v82, v82
	v_exp_f32_e32 v83, v83
	v_exp_f32_e32 v84, v84
	v_exp_f32_e32 v85, v85
	v_exp_f32_e32 v86, v86
	v_exp_f32_e32 v87, v87
	v_exp_f32_e32 v88, v88
	v_exp_f32_e32 v89, v89
	v_exp_f32_e32 v90, v90
	v_exp_f32_e32 v91, v91
	v_exp_f32_e32 v92, v92
	v_exp_f32_e32 v93, v93
	v_exp_f32_e32 v94, v94
	v_exp_f32_e32 v95, v95
	v_exp_f32_e32 v96, v96
	v_exp_f32_e32 v97, v97
	v_pk_add_f32 v[82:83], v[82:83], s[82:83]
	v_pk_add_f32 v[84:85], v[84:85], s[82:83]
	v_pk_add_f32 v[86:87], v[86:87], s[82:83]
	v_pk_add_f32 v[88:89], v[88:89], s[82:83]
	v_pk_add_f32 v[90:91], v[90:91], s[82:83]
	v_pk_add_f32 v[92:93], v[92:93], s[82:83]
	v_pk_add_f32 v[94:95], v[94:95], s[82:83]
	v_pk_add_f32 v[96:97], v[96:97], s[82:83]
	v_rcp_f32_e32 v82, v82
	v_rcp_f32_e32 v83, v83
	v_rcp_f32_e32 v84, v84
	v_rcp_f32_e32 v85, v85
	v_rcp_f32_e32 v86, v86
	v_rcp_f32_e32 v87, v87
	v_rcp_f32_e32 v88, v88
	v_rcp_f32_e32 v89, v89
	v_rcp_f32_e32 v90, v90
	v_rcp_f32_e32 v91, v91
	v_rcp_f32_e32 v92, v92
	v_rcp_f32_e32 v93, v93
	v_rcp_f32_e32 v94, v94
	v_rcp_f32_e32 v95, v95
	v_rcp_f32_e32 v96, v96
	v_rcp_f32_e32 v97, v97
	v_cvt_pk_f16_f32 v198, v82, v83
	v_cvt_pk_f16_f32 v199, v84, v85
	v_cvt_pk_f16_f32 v200, v86, v87
	v_cvt_pk_f16_f32 v201, v88, v89
	v_cvt_pk_f16_f32 v202, v90, v91
	v_cvt_pk_f16_f32 v203, v92, v93
	v_cvt_pk_f16_f32 v204, v94, v95
	v_cvt_pk_f16_f32 v205, v96, v97
	v_mfma_f32_32x32x16_f16 v[82:97], v[194:197], v[186:189], 0
	v_exp_f32_e32 v98, v98
	v_exp_f32_e32 v99, v99
	v_exp_f32_e32 v100, v100
	v_exp_f32_e32 v101, v101
	v_exp_f32_e32 v102, v102
	v_exp_f32_e32 v103, v103
	v_mfma_f32_32x32x16_f16 v[66:81], v[198:201], v[6:9], v[66:81]
	v_exp_f32_e32 v104, v104
	v_exp_f32_e32 v105, v105
	v_exp_f32_e32 v106, v106
	v_exp_f32_e32 v107, v107
	v_exp_f32_e32 v108, v108
	v_exp_f32_e32 v109, v109
	v_mfma_f32_32x32x16_f16 v[66:81], v[202:205], v[10:13], v[66:81]
	v_exp_f32_e32 v110, v110
	v_exp_f32_e32 v111, v111
	v_exp_f32_e32 v112, v112
	v_exp_f32_e32 v113, v113
	v_pk_add_f32 v[98:99], v[98:99], s[82:83]
	v_pk_add_f32 v[100:101], v[100:101], s[82:83]
	v_pk_add_f32 v[102:103], v[102:103], s[82:83]
	v_pk_add_f32 v[104:105], v[104:105], s[82:83]
	v_pk_add_f32 v[106:107], v[106:107], s[82:83]
	v_pk_add_f32 v[108:109], v[108:109], s[82:83]
	v_pk_add_f32 v[110:111], v[110:111], s[82:83]
	v_pk_add_f32 v[112:113], v[112:113], s[82:83]
	v_rcp_f32_e32 v98, v98
	v_rcp_f32_e32 v99, v99
	v_rcp_f32_e32 v100, v100
	v_rcp_f32_e32 v101, v101
	v_rcp_f32_e32 v102, v102
	v_rcp_f32_e32 v103, v103
	v_rcp_f32_e32 v104, v104
	v_rcp_f32_e32 v105, v105
	v_rcp_f32_e32 v106, v106
	v_rcp_f32_e32 v107, v107
	v_rcp_f32_e32 v108, v108
	v_rcp_f32_e32 v109, v109
	v_rcp_f32_e32 v110, v110
	v_rcp_f32_e32 v111, v111
	v_rcp_f32_e32 v112, v112
	v_rcp_f32_e32 v113, v113
	v_cvt_pk_f16_f32 v206, v98, v99
	v_cvt_pk_f16_f32 v207, v100, v101
	v_cvt_pk_f16_f32 v208, v102, v103
	v_cvt_pk_f16_f32 v209, v104, v105
	v_cvt_pk_f16_f32 v210, v106, v107
	v_cvt_pk_f16_f32 v211, v108, v109
	v_cvt_pk_f16_f32 v212, v110, v111
	v_cvt_pk_f16_f32 v213, v112, v113
	v_mfma_f32_32x32x16_f16 v[98:113], v[194:197], v[190:193], 0
	v_exp_f32_e32 v82, v82
	v_exp_f32_e32 v83, v83
	v_exp_f32_e32 v84, v84
	v_exp_f32_e32 v85, v85
	v_exp_f32_e32 v86, v86
	v_exp_f32_e32 v87, v87
	v_mfma_f32_32x32x16_f16 v[50:65], v[206:209], v[6:9], v[50:65]
	v_exp_f32_e32 v88, v88
	v_exp_f32_e32 v89, v89
	v_exp_f32_e32 v90, v90
	v_exp_f32_e32 v91, v91
	v_exp_f32_e32 v92, v92
	v_exp_f32_e32 v93, v93
	v_mfma_f32_32x32x16_f16 v[50:65], v[210:213], v[10:13], v[50:65]
	v_exp_f32_e32 v94, v94
	v_exp_f32_e32 v95, v95
	v_exp_f32_e32 v96, v96
	v_exp_f32_e32 v97, v97
	v_pk_add_f32 v[82:83], v[82:83], s[82:83]
	v_pk_add_f32 v[84:85], v[84:85], s[82:83]
	v_pk_add_f32 v[86:87], v[86:87], s[82:83]
	v_pk_add_f32 v[88:89], v[88:89], s[82:83]
	v_pk_add_f32 v[90:91], v[90:91], s[82:83]
	v_pk_add_f32 v[92:93], v[92:93], s[82:83]
	v_pk_add_f32 v[94:95], v[94:95], s[82:83]
	v_pk_add_f32 v[96:97], v[96:97], s[82:83]
	v_rcp_f32_e32 v82, v82
	v_rcp_f32_e32 v83, v83
	v_rcp_f32_e32 v84, v84
	v_rcp_f32_e32 v85, v85
	v_rcp_f32_e32 v86, v86
	v_rcp_f32_e32 v87, v87
	v_rcp_f32_e32 v88, v88
	v_rcp_f32_e32 v89, v89
	v_rcp_f32_e32 v90, v90
	v_rcp_f32_e32 v91, v91
	v_rcp_f32_e32 v92, v92
	v_rcp_f32_e32 v93, v93
	v_rcp_f32_e32 v94, v94
	v_rcp_f32_e32 v95, v95
	v_rcp_f32_e32 v96, v96
	v_rcp_f32_e32 v97, v97
	v_cvt_pk_f16_f32 v214, v82, v83
	v_cvt_pk_f16_f32 v215, v84, v85
	v_cvt_pk_f16_f32 v216, v86, v87
	v_cvt_pk_f16_f32 v217, v88, v89
	v_cvt_pk_f16_f32 v218, v90, v91
	v_cvt_pk_f16_f32 v219, v92, v93
	v_cvt_pk_f16_f32 v220, v94, v95
	v_cvt_pk_f16_f32 v221, v96, v97
	v_exp_f32_e32 v98, v98
	v_exp_f32_e32 v99, v99
	v_exp_f32_e32 v100, v100
	v_exp_f32_e32 v101, v101
	v_exp_f32_e32 v102, v102
	v_exp_f32_e32 v103, v103
	v_mfma_f32_32x32x16_f16 v[34:49], v[214:217], v[6:9], v[34:49]
	v_exp_f32_e32 v104, v104
	v_exp_f32_e32 v105, v105
	v_exp_f32_e32 v106, v106
	v_exp_f32_e32 v107, v107
	v_exp_f32_e32 v108, v108
	v_exp_f32_e32 v109, v109
	v_mfma_f32_32x32x16_f16 v[34:49], v[218:221], v[10:13], v[34:49]
	v_exp_f32_e32 v110, v110
	v_exp_f32_e32 v111, v111
	v_exp_f32_e32 v112, v112
	v_exp_f32_e32 v113, v113
	v_pk_add_f32 v[98:99], v[98:99], s[82:83]
	v_pk_add_f32 v[100:101], v[100:101], s[82:83]
	v_pk_add_f32 v[102:103], v[102:103], s[82:83]
	v_pk_add_f32 v[104:105], v[104:105], s[82:83]
	v_pk_add_f32 v[106:107], v[106:107], s[82:83]
	v_pk_add_f32 v[108:109], v[108:109], s[82:83]
	v_pk_add_f32 v[110:111], v[110:111], s[82:83]
	v_pk_add_f32 v[112:113], v[112:113], s[82:83]
	v_rcp_f32_e32 v98, v98
	v_rcp_f32_e32 v99, v99
	v_rcp_f32_e32 v100, v100
	v_rcp_f32_e32 v101, v101
	v_rcp_f32_e32 v102, v102
	v_rcp_f32_e32 v103, v103
	v_rcp_f32_e32 v104, v104
	v_rcp_f32_e32 v105, v105
	v_rcp_f32_e32 v106, v106
	v_rcp_f32_e32 v107, v107
	v_rcp_f32_e32 v108, v108
	v_rcp_f32_e32 v109, v109
	v_rcp_f32_e32 v110, v110
	v_rcp_f32_e32 v111, v111
	v_rcp_f32_e32 v112, v112
	v_rcp_f32_e32 v113, v113
	v_cvt_pk_f16_f32 v222, v98, v99
	v_cvt_pk_f16_f32 v223, v100, v101
	v_cvt_pk_f16_f32 v224, v102, v103
	v_cvt_pk_f16_f32 v225, v104, v105
	v_cvt_pk_f16_f32 v226, v106, v107
	v_cvt_pk_f16_f32 v227, v108, v109
	v_cvt_pk_f16_f32 v228, v110, v111
	v_cvt_pk_f16_f32 v229, v112, v113
	v_mfma_f32_32x32x16_f16 v[18:33], v[222:225], v[6:9], v[18:33]
	v_add_u32_e32 v194, s13, v243
	v_mfma_f32_32x32x16_f16 v[18:33], v[226:229], v[10:13], v[18:33]
	s_cmp_ge_i32 s18, s71
	s_cbranch_scc1 .Lflush
